# RMSNorm wave_sum: 6 ds_bpermute round trips per row replaced by DPP / permlane-swap adds in the same order (4 chains)
# baseline (speedup 1.0000x reference)
.LBB0_231:
	s_waitcnt vmcnt(0)
	v_lshlrev_b32_e32 v187, 16, v173
	v_lshlrev_b32_e32 v186, 16, v172
	v_and_b32_e32 v173, 0xffff0000, v173
	v_and_b32_e32 v172, 0xffff0000, v172
	v_pk_mul_f32 v[188:189], v[172:173], v[172:173]
	v_lshlrev_b32_e32 v191, 16, v169
	v_pk_fma_f32 v[188:189], v[186:187], v[186:187], v[188:189]
	v_lshlrev_b32_e32 v190, 16, v168
	v_and_b32_e32 v169, 0xffff0000, v169
	v_and_b32_e32 v168, 0xffff0000, v168
	v_lshlrev_b32_e32 v182, 16, v166
	v_and_b32_e32 v183, 0xffff0000, v166
	v_lshlrev_b32_e32 v184, 16, v170
	v_pk_add_f32 v[188:189], v[188:189], v[188:189] op_sel_hi:[0,1]
	v_pk_mul_f32 v[192:193], v[168:169], v[168:169]
	v_lshlrev_b32_e32 v166, 16, v167
	v_pk_fma_f32 v[192:193], v[190:191], v[190:191], v[192:193]
	v_mul_f32_e32 v185, v182, v182
	v_mul_f32_e32 v195, v183, v183
	v_and_b32_e32 v167, 0xffff0000, v167
	v_mul_f32_e32 v188, v166, v166
	v_mov_b32_e32 v194, v184
	v_and_b32_e32 v201, 0xffff0000, v170
	v_lshlrev_b32_e32 v170, 16, v171
	v_and_b32_e32 v171, 0xffff0000, v171
	v_pk_add_f32 v[192:193], v[192:193], v[192:193] op_sel_hi:[0,1]
	v_pk_fma_f32 v[196:197], v[166:167], v[166:167], v[188:189] op_sel_hi:[1,1,0]
	v_pk_add_f32 v[194:195], v[184:185], v[194:195]
	v_mul_f32_e32 v196, v201, v201
	v_mul_f32_e32 v192, v170, v170
	v_mul_f32_e32 v188, v171, v171
	v_mul_f32_e32 v198, v184, v184
	v_mov_b32_e32 v199, v195
	v_pk_add_f32 v[194:195], v[198:199], v[196:197]
	v_pk_add_f32 v[188:189], v[192:193], v[188:189]
	s_add_i32 s10, s21, s25
	v_pk_add_f32 v[188:189], v[194:195], v[188:189]
	s_cmp_lt_i32 s10, s15
	v_add_f32_e32 v185, v188, v189
	s_cselect_b32 s10, s10, s25
	s_ashr_i32 s11, s10, 31
	s_lshl_b64 s[10:11], s[10:11], 11
	v_lshl_add_u64 v[164:165], v[144:145], 0, s[10:11]
	s_nop 1
	v_add_f32_dpp v185, v185, v185 quad_perm:[1,0,3,2] row_mask:0xf bank_mask:0xf
	global_load_dwordx2 v[158:159], v[164:165], off
	global_load_dwordx2 v[160:161], v[164:165], off offset:512
	global_load_dwordx2 v[162:163], v[164:165], off offset:1024
	s_nop 0
	global_load_dwordx2 v[164:165], v[164:165], off offset:1536
	v_mov_b32_e32 v195, v172
	v_mov_b32_e32 v172, v187
	s_nop 1
	v_add_f32_dpp v185, v185, v185 quad_perm:[2,3,0,1] row_mask:0xf bank_mask:0xf
	s_nop 1
	v_add_f32_dpp v185, v185, v185 row_half_mirror row_mask:0xf bank_mask:0xf
	s_nop 1
	v_add_f32_dpp v185, v185, v185 row_mirror row_mask:0xf bank_mask:0xf
	v_mov_b32_e32 v188, v185
	s_nop 1
	v_permlane16_swap_b32_e32 v185, v188
	v_add_f32_e32 v185, v185, v188
	v_mov_b32_e32 v188, v185
	s_nop 1
	v_permlane32_swap_b32_e32 v185, v188
	v_add_f32_e32 v185, v185, v188
	v_fmamk_f32 v185, v185, 0x3a800000, v222
	v_cmp_gt_f32_e32 vcc, s78, v185
	v_mul_f32_e32 v188, 0x4f800000, v185
	s_nop 0
	v_cndmask_b32_e32 v185, v185, v188, vcc
	v_sqrt_f32_e32 v188, v185
	s_nop 0
	v_add_u32_e32 v189, -1, v188
	v_fma_f32 v192, -v189, v188, v185
	v_cmp_ge_f32_e64 s[10:11], 0, v192
	v_add_u32_e32 v192, 1, v188
	s_nop 0
	v_cndmask_b32_e64 v189, v188, v189, s[10:11]
	v_fma_f32 v188, -v192, v188, v185
	v_cmp_lt_f32_e64 s[10:11], 0, v188
	s_nop 1
	v_cndmask_b32_e64 v188, v189, v192, s[10:11]
	v_mul_f32_e32 v189, 0x37800000, v188
	v_cndmask_b32_e32 v188, v188, v189, vcc
	v_cmp_class_f32_e32 vcc, v185, v223
	s_nop 1
	v_cndmask_b32_e32 v185, v188, v185, vcc
	v_div_scale_f32 v188, s[10:11], v185, v185, 1.0
	v_rcp_f32_e32 v189, v188
	s_nop 0
	v_fma_f32 v192, -v188, v189, 1.0
	v_fmac_f32_e32 v189, v192, v189
	v_div_scale_f32 v192, vcc, 1.0, v185, 1.0
	v_mul_f32_e32 v193, v192, v189
	v_fma_f32 v194, -v188, v193, v192
	v_fmac_f32_e32 v193, v194, v189
	v_fma_f32 v188, -v188, v193, v192
	v_div_fmas_f32 v188, v188, v189, v193
	v_div_fixup_f32 v188, v188, v185, 1.0
	v_mov_b32_e32 v194, v186
	v_lshl_add_u64 v[192:193], s[12:13], 0, v[156:157]
	v_pk_mul_f32 v[194:195], v[188:189], v[194:195] op_sel_hi:[0,1]
	v_pk_mul_f32 v[172:173], v[188:189], v[172:173] op_sel_hi:[0,1]
	v_pk_mul_f32 v[172:173], v[2:3], v[172:173]
	v_pk_mul_f32 v[186:187], v[0:1], v[194:195]
	v_add_co_u32_e32 v192, vcc, s38, v192
	v_cvt_pk_bf16_f32 v194, v186, v187
	v_cvt_pk_bf16_f32 v195, v172, v173
	v_addc_co_u32_e32 v193, vcc, 0, v193, vcc
	global_store_dwordx2 v[192:193], v[194:195], off
	v_mov_b32_e32 v194, v190
	v_mov_b32_e32 v195, v168
	v_mov_b32_e32 v168, v191
	v_pk_mul_f32 v[194:195], v[188:189], v[194:195] op_sel_hi:[0,1]
	v_pk_mul_f32 v[168:169], v[188:189], v[168:169] op_sel_hi:[0,1]
	v_mov_b32_e32 v185, v201
	v_pk_mul_f32 v[168:169], v[6:7], v[168:169]
	v_pk_mul_f32 v[190:191], v[4:5], v[194:195]
	v_pk_mul_f32 v[182:183], v[182:183], v[188:189] op_sel_hi:[1,0]
	v_pk_mul_f32 v[166:167], v[166:167], v[188:189] op_sel_hi:[1,0]
	v_pk_mul_f32 v[184:185], v[184:185], v[188:189] op_sel_hi:[1,0]
	v_pk_mul_f32 v[170:171], v[170:171], v[188:189] op_sel_hi:[1,0]
	v_cvt_pk_bf16_f32 v194, v190, v191
	v_cvt_pk_bf16_f32 v195, v168, v169
	v_pk_mul_f32 v[166:167], v[10:11], v[166:167]
	v_pk_mul_f32 v[182:183], v[8:9], v[182:183]
	v_pk_mul_f32 v[170:171], v[14:15], v[170:171]
	v_pk_mul_f32 v[184:185], v[12:13], v[184:185]
	global_store_dwordx2 v[192:193], v[194:195], off offset:512
	v_cvt_pk_bf16_f32 v194, v182, v183
	v_cvt_pk_bf16_f32 v195, v166, v167
	v_cvt_pk_bf16_f32 v188, v184, v185
	v_cvt_pk_bf16_f32 v189, v170, v171
	global_store_dwordx2 v[192:193], v[194:195], off offset:1024
	global_store_dwordx2 v[192:193], v[188:189], off offset:1536
	v_pk_fma_f32 v[188:189], v[16:17], v[186:187], 0 op_sel_hi:[1,0,0]
	v_pk_fma_f32 v[192:193], v[18:19], v[186:187], 0 op_sel_hi:[1,0,0]
	v_pk_fma_f32 v[194:195], v[24:25], v[186:187], 0 op_sel_hi:[1,0,0]
	v_pk_fma_f32 v[196:197], v[26:27], v[186:187], 0 op_sel_hi:[1,0,0]
	v_pk_fma_f32 v[192:193], v[22:23], v[186:187], v[192:193] op_sel:[0,1,0]
	v_pk_fma_f32 v[188:189], v[20:21], v[186:187], v[188:189] op_sel:[0,1,0]
	v_pk_fma_f32 v[196:197], v[30:31], v[186:187], v[196:197] op_sel:[0,1,0]
	v_pk_fma_f32 v[186:187], v[28:29], v[186:187], v[194:195] op_sel:[0,1,0]
	v_pk_fma_f32 v[188:189], v[32:33], v[172:173], v[188:189] op_sel_hi:[1,0,1]
	v_pk_fma_f32 v[192:193], v[34:35], v[172:173], v[192:193] op_sel_hi:[1,0,1]
	v_pk_fma_f32 v[186:187], v[40:41], v[172:173], v[186:187] op_sel_hi:[1,0,1]
	v_pk_fma_f32 v[194:195], v[42:43], v[172:173], v[196:197] op_sel_hi:[1,0,1]
	v_pk_fma_f32 v[192:193], v[38:39], v[172:173], v[192:193] op_sel:[0,1,0]
	v_pk_fma_f32 v[188:189], v[36:37], v[172:173], v[188:189] op_sel:[0,1,0]
	v_pk_fma_f32 v[194:195], v[46:47], v[172:173], v[194:195] op_sel:[0,1,0]
	v_pk_fma_f32 v[172:173], v[44:45], v[172:173], v[186:187] op_sel:[0,1,0]
	v_pk_fma_f32 v[186:187], v[48:49], v[190:191], v[188:189] op_sel_hi:[1,0,1]
	v_pk_fma_f32 v[188:189], v[50:51], v[190:191], v[192:193] op_sel_hi:[1,0,1]
	v_pk_fma_f32 v[172:173], v[56:57], v[190:191], v[172:173] op_sel_hi:[1,0,1]
	v_pk_fma_f32 v[192:193], v[58:59], v[190:191], v[194:195] op_sel_hi:[1,0,1]
	v_pk_fma_f32 v[188:189], v[54:55], v[190:191], v[188:189] op_sel:[0,1,0]
	v_pk_fma_f32 v[186:187], v[52:53], v[190:191], v[186:187] op_sel:[0,1,0]
	v_pk_fma_f32 v[192:193], v[62:63], v[190:191], v[192:193] op_sel:[0,1,0]
	v_pk_fma_f32 v[172:173], v[60:61], v[190:191], v[172:173] op_sel:[0,1,0]
	v_pk_fma_f32 v[186:187], v[64:65], v[168:169], v[186:187] op_sel_hi:[1,0,1]
	v_pk_fma_f32 v[188:189], v[66:67], v[168:169], v[188:189] op_sel_hi:[1,0,1]
	v_pk_fma_f32 v[172:173], v[72:73], v[168:169], v[172:173] op_sel_hi:[1,0,1]
	v_pk_fma_f32 v[190:191], v[74:75], v[168:169], v[192:193] op_sel_hi:[1,0,1]
	v_pk_fma_f32 v[188:189], v[70:71], v[168:169], v[188:189] op_sel:[0,1,0]
	v_pk_fma_f32 v[186:187], v[68:69], v[168:169], v[186:187] op_sel:[0,1,0]
	v_pk_fma_f32 v[190:191], v[78:79], v[168:169], v[190:191] op_sel:[0,1,0]
	v_pk_fma_f32 v[168:169], v[76:77], v[168:169], v[172:173] op_sel:[0,1,0]
	v_pk_fma_f32 v[172:173], v[80:81], v[182:183], v[186:187] op_sel_hi:[1,0,1]
	v_pk_fma_f32 v[186:187], v[82:83], v[182:183], v[188:189] op_sel_hi:[1,0,1]
	v_pk_fma_f32 v[168:169], v[88:89], v[182:183], v[168:169] op_sel_hi:[1,0,1]
	v_pk_fma_f32 v[188:189], v[90:91], v[182:183], v[190:191] op_sel_hi:[1,0,1]
	v_pk_fma_f32 v[186:187], v[86:87], v[182:183], v[186:187] op_sel:[0,1,0]
	v_pk_fma_f32 v[172:173], v[84:85], v[182:183], v[172:173] op_sel:[0,1,0]
	v_pk_fma_f32 v[188:189], v[94:95], v[182:183], v[188:189] op_sel:[0,1,0]
	v_pk_fma_f32 v[168:169], v[92:93], v[182:183], v[168:169] op_sel:[0,1,0]
	v_pk_fma_f32 v[172:173], v[96:97], v[166:167], v[172:173] op_sel_hi:[1,0,1]
	v_pk_fma_f32 v[182:183], v[98:99], v[166:167], v[186:187] op_sel_hi:[1,0,1]
	v_pk_fma_f32 v[168:169], v[104:105], v[166:167], v[168:169] op_sel_hi:[1,0,1]
	v_pk_fma_f32 v[186:187], v[106:107], v[166:167], v[188:189] op_sel_hi:[1,0,1]
	v_pk_fma_f32 v[182:183], v[102:103], v[166:167], v[182:183] op_sel:[0,1,0]
	v_pk_fma_f32 v[172:173], v[100:101], v[166:167], v[172:173] op_sel:[0,1,0]
	v_pk_fma_f32 v[186:187], v[110:111], v[166:167], v[186:187] op_sel:[0,1,0]
	v_pk_fma_f32 v[166:167], v[108:109], v[166:167], v[168:169] op_sel:[0,1,0]
	v_pk_fma_f32 v[168:169], v[112:113], v[184:185], v[172:173] op_sel_hi:[1,0,1]
	v_pk_fma_f32 v[166:167], v[120:121], v[184:185], v[166:167] op_sel_hi:[1,0,1]
	v_pk_fma_f32 v[172:173], v[114:115], v[184:185], v[182:183] op_sel_hi:[1,0,1]
	v_pk_fma_f32 v[182:183], v[122:123], v[184:185], v[186:187] op_sel_hi:[1,0,1]
	v_pk_fma_f32 v[168:169], v[116:117], v[184:185], v[168:169] op_sel:[0,1,0]
	v_pk_fma_f32 v[166:167], v[124:125], v[184:185], v[166:167] op_sel:[0,1,0]
	v_pk_fma_f32 v[172:173], v[118:119], v[184:185], v[172:173] op_sel:[0,1,0]
	v_pk_fma_f32 v[182:183], v[126:127], v[184:185], v[182:183] op_sel:[0,1,0]
	v_pk_fma_f32 v[168:169], v[128:129], v[170:171], v[168:169] op_sel_hi:[1,0,1]
	v_pk_fma_f32 v[166:167], v[136:137], v[170:171], v[166:167] op_sel_hi:[1,0,1]
	v_pk_fma_f32 v[172:173], v[130:131], v[170:171], v[172:173] op_sel_hi:[1,0,1]
	v_pk_fma_f32 v[182:183], v[138:139], v[170:171], v[182:183] op_sel_hi:[1,0,1]
	v_pk_fma_f32 v[168:169], v[132:133], v[170:171], v[168:169] op_sel:[0,1,0]
	v_pk_fma_f32 v[166:167], v[140:141], v[170:171], v[166:167] op_sel:[0,1,0]
	v_pk_fma_f32 v[172:173], v[134:135], v[170:171], v[172:173] op_sel:[0,1,0]
	v_pk_fma_f32 v[182:183], v[142:143], v[170:171], v[182:183] op_sel:[0,1,0]
	v_cndmask_b32_e64 v170, v168, v166, s[6:7]
	v_cndmask_b32_e64 v166, v166, v168, s[6:7]
	ds_bpermute_b32 v166, v181, v166
	v_cndmask_b32_e64 v168, v169, v167, s[6:7]
	v_cndmask_b32_e64 v167, v167, v169, s[6:7]
	ds_bpermute_b32 v167, v181, v167
	v_cndmask_b32_e64 v169, v182, v172, s[6:7]
	s_waitcnt lgkmcnt(1)
	v_add_f32_e32 v166, v170, v166
	ds_bpermute_b32 v169, v181, v169
	v_cndmask_b32_e64 v170, v183, v173, s[6:7]
	ds_bpermute_b32 v170, v181, v170
	s_waitcnt lgkmcnt(2)
	v_add_f32_e32 v167, v168, v167
	v_cndmask_b32_e64 v168, v172, v182, s[6:7]
	s_waitcnt lgkmcnt(1)
	v_add_f32_e32 v168, v168, v169
	v_cndmask_b32_e64 v169, v173, v183, s[6:7]
	s_waitcnt lgkmcnt(0)
	v_add_f32_e32 v169, v169, v170
	v_cndmask_b32_e64 v170, v166, v168, s[0:1]
	v_cndmask_b32_e64 v166, v168, v166, s[0:1]
	v_cndmask_b32_e64 v168, v167, v169, s[0:1]
	v_cndmask_b32_e64 v167, v169, v167, s[0:1]
	ds_bpermute_b32 v166, v180, v166
	ds_bpermute_b32 v167, v180, v167
	s_waitcnt lgkmcnt(1)
	v_add_f32_e32 v166, v170, v166
	s_waitcnt lgkmcnt(0)
	v_add_f32_e32 v167, v168, v167
	v_cndmask_b32_e64 v168, v166, v167, s[2:3]
	v_cndmask_b32_e64 v166, v167, v166, s[2:3]
	ds_bpermute_b32 v166, v179, v166
	s_waitcnt lgkmcnt(0)
	v_add_f32_e32 v166, v168, v166
	ds_bpermute_b32 v167, v178, v166
	s_waitcnt lgkmcnt(0)
	v_add_f32_e32 v166, v166, v167
	ds_bpermute_b32 v167, v177, v166
	s_waitcnt lgkmcnt(0)
	v_add_f32_e32 v166, v166, v167
	ds_bpermute_b32 v167, v176, v166
	s_and_saveexec_b64 s[10:11], s[4:5]
	s_cbranch_execz .LBB0_230
	v_lshl_add_u64 v[168:169], s[12:13], 0, v[154:155]
	s_waitcnt lgkmcnt(0)
	v_add_f32_e32 v166, v166, v167
	global_store_dword v[168:169], v166, off
	s_branch .LBB0_230

.LBB0_238:
	s_add_i32 s8, s21, s22
	s_cmp_lt_i32 s8, s15
	s_cselect_b32 s8, s8, s22
	s_ashr_i32 s9, s8, 31
	s_lshl_b64 s[8:9], s[8:9], 12
	v_lshl_add_u64 v[172:173], v[192:193], 0, s[8:9]
	v_lshl_add_u64 v[198:199], s[12:13], 0, v[196:197]
	s_mov_b32 s8, 0x26d00000
	v_add_co_u32_e32 v212, vcc, s8, v198
	s_waitcnt vmcnt(0)
	v_cvt_pk_bf16_f32 v210, v188, v189
	v_cvt_pk_bf16_f32 v211, v190, v191
	v_addc_co_u32_e32 v213, vcc, 0, v199, vcc
	global_load_dwordx4 v[160:163], v[172:173], off
	global_load_dwordx4 v[164:167], v[172:173], off offset:1024
	global_load_dwordx4 v[168:171], v[172:173], off offset:2048
	s_nop 0
	global_load_dwordx4 v[172:175], v[172:173], off offset:3072
	v_pk_mul_f32 v[214:215], v[190:191], v[190:191]
	global_store_dwordx2 v[212:213], v[210:211], off
	v_cvt_pk_bf16_f32 v210, v184, v185
	v_cvt_pk_bf16_f32 v211, v186, v187
	global_store_dwordx2 v[212:213], v[210:211], off offset:512
	v_cvt_pk_bf16_f32 v210, v180, v181
	v_cvt_pk_bf16_f32 v211, v182, v183
	global_store_dwordx2 v[212:213], v[210:211], off offset:1024
	v_cvt_pk_bf16_f32 v210, v176, v177
	v_cvt_pk_bf16_f32 v211, v178, v179
	v_pk_mul_f32 v[216:217], v[188:189], v[188:189]
	global_store_dwordx2 v[212:213], v[210:211], off offset:1536
	v_pk_mul_f32 v[210:211], v[186:187], v[186:187]
	v_pk_mul_f32 v[212:213], v[184:185], v[184:185]
	v_pk_mov_b32 v[218:219], v[216:217], v[214:215] op_sel:[1,0]
	v_mov_b32_e32 v217, v215
	v_pk_add_f32 v[214:215], v[218:219], v[216:217]
	v_pk_mov_b32 v[216:217], v[212:213], v[210:211] op_sel:[1,0]
	v_mov_b32_e32 v213, v211
	v_pk_add_f32 v[210:211], v[216:217], v[212:213]
	v_pk_add_f32 v[214:215], v[214:215], v[214:215] op_sel_hi:[0,1]
	v_pk_add_f32 v[210:211], v[210:211], v[210:211] op_sel_hi:[0,1]
	v_mul_f32_e32 v210, v180, v180
	v_pk_fma_f32 v[212:213], v[180:181], v[180:181], v[210:211] op_sel_hi:[1,1,0]
	v_mul_f32_e32 v210, v182, v182
	v_pk_fma_f32 v[216:217], v[182:183], v[182:183], v[210:211] op_sel_hi:[1,1,0]
	v_mul_f32_e32 v212, v176, v176
	v_mul_f32_e32 v216, v177, v177
	v_mul_f32_e32 v214, v178, v178
	v_mul_f32_e32 v210, v179, v179
	v_pk_add_f32 v[212:213], v[212:213], v[216:217]
	v_pk_add_f32 v[210:211], v[214:215], v[210:211]
	s_nop 0
	v_pk_add_f32 v[210:211], v[212:213], v[210:211]
	s_nop 0
	v_add_f32_e32 v207, v210, v211
	s_nop 1
	v_add_f32_dpp v207, v207, v207 quad_perm:[1,0,3,2] row_mask:0xf bank_mask:0xf
	s_nop 1
	v_add_f32_dpp v207, v207, v207 quad_perm:[2,3,0,1] row_mask:0xf bank_mask:0xf
	s_nop 1
	v_add_f32_dpp v207, v207, v207 row_half_mirror row_mask:0xf bank_mask:0xf
	s_nop 1
	v_add_f32_dpp v207, v207, v207 row_mirror row_mask:0xf bank_mask:0xf
	v_mov_b32_e32 v210, v207
	s_nop 1
	v_permlane16_swap_b32_e32 v207, v210
	v_add_f32_e32 v207, v207, v210
	v_mov_b32_e32 v210, v207
	s_nop 1
	v_permlane32_swap_b32_e32 v207, v210
	v_add_f32_e32 v207, v207, v210
	v_fmamk_f32 v207, v207, 0x3a800000, v222
	v_cmp_gt_f32_e32 vcc, s78, v207
	v_mul_f32_e32 v210, 0x4f800000, v207
	s_nop 0
	v_cndmask_b32_e32 v207, v207, v210, vcc
	v_sqrt_f32_e32 v210, v207
	s_nop 0
	v_add_u32_e32 v211, -1, v210
	v_fma_f32 v212, -v211, v210, v207
	v_cmp_ge_f32_e64 s[8:9], 0, v212
	v_add_u32_e32 v212, 1, v210
	s_nop 0
	v_cndmask_b32_e64 v211, v210, v211, s[8:9]
	v_fma_f32 v210, -v212, v210, v207
	v_cmp_lt_f32_e64 s[8:9], 0, v210
	s_nop 1
	v_cndmask_b32_e64 v210, v211, v212, s[8:9]
	v_mul_f32_e32 v211, 0x37800000, v210
	v_cndmask_b32_e32 v210, v210, v211, vcc
	v_cmp_class_f32_e32 vcc, v207, v223
	s_nop 1
	v_cndmask_b32_e32 v207, v210, v207, vcc
	v_div_scale_f32 v210, s[8:9], v207, v207, 1.0
	v_rcp_f32_e32 v211, v210
	s_nop 0
	v_fma_f32 v212, -v210, v211, 1.0
	v_fmac_f32_e32 v211, v212, v211
	v_div_scale_f32 v212, vcc, 1.0, v207, 1.0
	v_mul_f32_e32 v213, v212, v211
	v_fma_f32 v214, -v210, v213, v212
	v_fmac_f32_e32 v213, v214, v211
	v_fma_f32 v210, -v210, v213, v212
	v_div_fmas_f32 v210, v210, v211, v213
	v_div_fixup_f32 v210, v210, v207, 1.0
	v_pk_mul_f32 v[188:189], v[188:189], v[210:211] op_sel_hi:[1,0]
	v_pk_mul_f32 v[190:191], v[190:191], v[210:211] op_sel_hi:[1,0]
	v_pk_mul_f32 v[188:189], v[0:1], v[188:189]
	v_pk_mul_f32 v[190:191], v[2:3], v[190:191]
	v_add_co_u32_e32 v198, vcc, s38, v198
	v_pk_mul_f32 v[184:185], v[184:185], v[210:211] op_sel_hi:[1,0]
	v_pk_mul_f32 v[186:187], v[186:187], v[210:211] op_sel_hi:[1,0]
	v_cvt_pk_bf16_f32 v212, v188, v189
	v_cvt_pk_bf16_f32 v213, v190, v191
	v_addc_co_u32_e32 v199, vcc, 0, v199, vcc
	v_pk_mul_f32 v[186:187], v[6:7], v[186:187]
	v_pk_mul_f32 v[184:185], v[4:5], v[184:185]
	v_pk_mul_f32 v[180:181], v[180:181], v[210:211] op_sel_hi:[1,0]
	v_pk_mul_f32 v[182:183], v[182:183], v[210:211] op_sel_hi:[1,0]
	v_pk_mul_f32 v[176:177], v[176:177], v[210:211] op_sel_hi:[1,0]
	v_pk_mul_f32 v[178:179], v[178:179], v[210:211] op_sel_hi:[1,0]
	global_store_dwordx2 v[198:199], v[212:213], off
	v_cvt_pk_bf16_f32 v212, v184, v185
	v_cvt_pk_bf16_f32 v213, v186, v187
	v_pk_mul_f32 v[182:183], v[10:11], v[182:183]
	v_pk_mul_f32 v[180:181], v[8:9], v[180:181]
	v_pk_mul_f32 v[178:179], v[14:15], v[178:179]
	v_pk_mul_f32 v[176:177], v[12:13], v[176:177]
	global_store_dwordx2 v[198:199], v[212:213], off offset:512
	v_cvt_pk_bf16_f32 v212, v180, v181
	v_cvt_pk_bf16_f32 v213, v182, v183
	v_cvt_pk_bf16_f32 v210, v176, v177
	v_cvt_pk_bf16_f32 v211, v178, v179
	global_store_dwordx2 v[198:199], v[212:213], off offset:1024
	global_store_dwordx2 v[198:199], v[210:211], off offset:1536
	v_pk_fma_f32 v[198:199], v[16:17], v[188:189], 0 op_sel_hi:[1,0,0]
	v_pk_fma_f32 v[210:211], v[18:19], v[188:189], 0 op_sel_hi:[1,0,0]
	v_pk_fma_f32 v[212:213], v[24:25], v[188:189], 0 op_sel_hi:[1,0,0]
	v_pk_fma_f32 v[214:215], v[26:27], v[188:189], 0 op_sel_hi:[1,0,0]
	v_pk_fma_f32 v[210:211], v[22:23], v[188:189], v[210:211] op_sel:[0,1,0]
	v_pk_fma_f32 v[198:199], v[20:21], v[188:189], v[198:199] op_sel:[0,1,0]
	v_pk_fma_f32 v[214:215], v[30:31], v[188:189], v[214:215] op_sel:[0,1,0]
	v_pk_fma_f32 v[188:189], v[28:29], v[188:189], v[212:213] op_sel:[0,1,0]
	v_pk_fma_f32 v[198:199], v[32:33], v[190:191], v[198:199] op_sel_hi:[1,0,1]
	v_pk_fma_f32 v[210:211], v[34:35], v[190:191], v[210:211] op_sel_hi:[1,0,1]
	v_pk_fma_f32 v[188:189], v[40:41], v[190:191], v[188:189] op_sel_hi:[1,0,1]
	v_pk_fma_f32 v[212:213], v[42:43], v[190:191], v[214:215] op_sel_hi:[1,0,1]
	v_pk_fma_f32 v[210:211], v[38:39], v[190:191], v[210:211] op_sel:[0,1,0]
	v_pk_fma_f32 v[198:199], v[36:37], v[190:191], v[198:199] op_sel:[0,1,0]
	v_pk_fma_f32 v[212:213], v[46:47], v[190:191], v[212:213] op_sel:[0,1,0]
	v_pk_fma_f32 v[188:189], v[44:45], v[190:191], v[188:189] op_sel:[0,1,0]
	v_pk_fma_f32 v[190:191], v[48:49], v[184:185], v[198:199] op_sel_hi:[1,0,1]
	v_pk_fma_f32 v[198:199], v[50:51], v[184:185], v[210:211] op_sel_hi:[1,0,1]
	v_pk_fma_f32 v[188:189], v[56:57], v[184:185], v[188:189] op_sel_hi:[1,0,1]
	v_pk_fma_f32 v[210:211], v[58:59], v[184:185], v[212:213] op_sel_hi:[1,0,1]
	v_pk_fma_f32 v[198:199], v[54:55], v[184:185], v[198:199] op_sel:[0,1,0]
	v_pk_fma_f32 v[190:191], v[52:53], v[184:185], v[190:191] op_sel:[0,1,0]
	v_pk_fma_f32 v[210:211], v[62:63], v[184:185], v[210:211] op_sel:[0,1,0]
	v_pk_fma_f32 v[184:185], v[60:61], v[184:185], v[188:189] op_sel:[0,1,0]
	v_pk_fma_f32 v[188:189], v[64:65], v[186:187], v[190:191] op_sel_hi:[1,0,1]
	v_pk_fma_f32 v[190:191], v[66:67], v[186:187], v[198:199] op_sel_hi:[1,0,1]
	v_pk_fma_f32 v[184:185], v[72:73], v[186:187], v[184:185] op_sel_hi:[1,0,1]
	v_pk_fma_f32 v[198:199], v[74:75], v[186:187], v[210:211] op_sel_hi:[1,0,1]
	v_pk_fma_f32 v[190:191], v[70:71], v[186:187], v[190:191] op_sel:[0,1,0]
	v_pk_fma_f32 v[188:189], v[68:69], v[186:187], v[188:189] op_sel:[0,1,0]
	v_pk_fma_f32 v[198:199], v[78:79], v[186:187], v[198:199] op_sel:[0,1,0]
	v_pk_fma_f32 v[184:185], v[76:77], v[186:187], v[184:185] op_sel:[0,1,0]
	v_pk_fma_f32 v[186:187], v[80:81], v[180:181], v[188:189] op_sel_hi:[1,0,1]
	v_pk_fma_f32 v[188:189], v[82:83], v[180:181], v[190:191] op_sel_hi:[1,0,1]
	v_pk_fma_f32 v[184:185], v[88:89], v[180:181], v[184:185] op_sel_hi:[1,0,1]
	v_pk_fma_f32 v[190:191], v[90:91], v[180:181], v[198:199] op_sel_hi:[1,0,1]
	v_pk_fma_f32 v[188:189], v[86:87], v[180:181], v[188:189] op_sel:[0,1,0]
	v_pk_fma_f32 v[186:187], v[84:85], v[180:181], v[186:187] op_sel:[0,1,0]
	v_pk_fma_f32 v[190:191], v[94:95], v[180:181], v[190:191] op_sel:[0,1,0]
	v_pk_fma_f32 v[180:181], v[92:93], v[180:181], v[184:185] op_sel:[0,1,0]
	v_pk_fma_f32 v[184:185], v[96:97], v[182:183], v[186:187] op_sel_hi:[1,0,1]
	v_pk_fma_f32 v[186:187], v[98:99], v[182:183], v[188:189] op_sel_hi:[1,0,1]
	v_pk_fma_f32 v[180:181], v[104:105], v[182:183], v[180:181] op_sel_hi:[1,0,1]
	v_pk_fma_f32 v[188:189], v[106:107], v[182:183], v[190:191] op_sel_hi:[1,0,1]
	v_pk_fma_f32 v[186:187], v[102:103], v[182:183], v[186:187] op_sel:[0,1,0]
	v_pk_fma_f32 v[184:185], v[100:101], v[182:183], v[184:185] op_sel:[0,1,0]
	v_pk_fma_f32 v[188:189], v[110:111], v[182:183], v[188:189] op_sel:[0,1,0]
	v_pk_fma_f32 v[180:181], v[108:109], v[182:183], v[180:181] op_sel:[0,1,0]
	v_pk_fma_f32 v[182:183], v[112:113], v[176:177], v[184:185] op_sel_hi:[1,0,1]
	v_pk_fma_f32 v[184:185], v[114:115], v[176:177], v[186:187] op_sel_hi:[1,0,1]
	v_pk_fma_f32 v[180:181], v[120:121], v[176:177], v[180:181] op_sel_hi:[1,0,1]
	v_pk_fma_f32 v[186:187], v[122:123], v[176:177], v[188:189] op_sel_hi:[1,0,1]
	v_pk_fma_f32 v[184:185], v[118:119], v[176:177], v[184:185] op_sel:[0,1,0]
	v_pk_fma_f32 v[182:183], v[116:117], v[176:177], v[182:183] op_sel:[0,1,0]
	v_pk_fma_f32 v[186:187], v[126:127], v[176:177], v[186:187] op_sel:[0,1,0]
	v_pk_fma_f32 v[176:177], v[124:125], v[176:177], v[180:181] op_sel:[0,1,0]
	v_pk_fma_f32 v[180:181], v[128:129], v[178:179], v[182:183] op_sel_hi:[1,0,1]
	v_pk_fma_f32 v[176:177], v[136:137], v[178:179], v[176:177] op_sel_hi:[1,0,1]
	v_pk_fma_f32 v[182:183], v[130:131], v[178:179], v[184:185] op_sel_hi:[1,0,1]
	v_pk_fma_f32 v[184:185], v[138:139], v[178:179], v[186:187] op_sel_hi:[1,0,1]
	v_pk_fma_f32 v[180:181], v[132:133], v[178:179], v[180:181] op_sel:[0,1,0]
	v_pk_fma_f32 v[176:177], v[140:141], v[178:179], v[176:177] op_sel:[0,1,0]
	v_pk_fma_f32 v[182:183], v[134:135], v[178:179], v[182:183] op_sel:[0,1,0]
	v_pk_fma_f32 v[184:185], v[142:143], v[178:179], v[184:185] op_sel:[0,1,0]
	v_cndmask_b32_e64 v178, v180, v176, s[6:7]
	v_cndmask_b32_e64 v176, v176, v180, s[6:7]
	ds_bpermute_b32 v176, v206, v176
	v_cndmask_b32_e64 v179, v184, v182, s[6:7]
	ds_bpermute_b32 v179, v206, v179
	v_cndmask_b32_e64 v180, v185, v183, s[6:7]
	ds_bpermute_b32 v180, v206, v180
	s_waitcnt lgkmcnt(2)
	v_add_f32_e32 v176, v178, v176
	v_cndmask_b32_e64 v178, v181, v177, s[6:7]
	v_cndmask_b32_e64 v177, v177, v181, s[6:7]
	ds_bpermute_b32 v177, v206, v177
	s_waitcnt lgkmcnt(0)
	v_add_f32_e32 v177, v178, v177
	v_cndmask_b32_e64 v178, v182, v184, s[6:7]
	v_add_f32_e32 v178, v178, v179
	v_cndmask_b32_e64 v179, v183, v185, s[6:7]
	v_add_f32_e32 v179, v179, v180
	v_cndmask_b32_e64 v180, v176, v178, s[0:1]
	v_cndmask_b32_e64 v176, v178, v176, s[0:1]
	v_cndmask_b32_e64 v178, v177, v179, s[0:1]
	v_cndmask_b32_e64 v177, v179, v177, s[0:1]
	ds_bpermute_b32 v176, v205, v176
	ds_bpermute_b32 v177, v205, v177
	s_waitcnt lgkmcnt(1)
	v_add_f32_e32 v176, v180, v176
	s_waitcnt lgkmcnt(0)
	v_add_f32_e32 v177, v178, v177
	v_cndmask_b32_e64 v178, v176, v177, s[2:3]
	v_cndmask_b32_e64 v176, v177, v176, s[2:3]
	ds_bpermute_b32 v176, v204, v176
	s_waitcnt lgkmcnt(0)
	v_add_f32_e32 v176, v178, v176
	ds_bpermute_b32 v177, v203, v176
	s_waitcnt lgkmcnt(0)
	v_add_f32_e32 v176, v176, v177
	ds_bpermute_b32 v177, v202, v176
	s_waitcnt lgkmcnt(0)
	v_add_f32_e32 v176, v176, v177
	ds_bpermute_b32 v177, v201, v176
	s_and_saveexec_b64 s[8:9], s[4:5]
	s_cbranch_execz .LBB0_237
	v_lshl_add_u64 v[178:179], s[12:13], 0, v[194:195]
	s_waitcnt lgkmcnt(0)
	v_add_f32_e32 v176, v176, v177
	global_store_dword v[178:179], v176, off
	s_branch .LBB0_237

.LBB0_242:
	s_add_i32 s4, s14, s20
	v_pk_mul_f32 v[46:47], v[22:23], v[22:23]
	v_pk_mul_f32 v[48:49], v[20:21], v[20:21]
	v_pk_mul_f32 v[50:51], v[18:19], v[18:19]
	v_pk_mul_f32 v[52:53], v[16:17], v[16:17]
	s_cmpk_lt_i32 s4, 0x1000
	v_mul_f32_e32 v54, v28, v28
	v_mul_f32_e32 v56, v30, v30
	v_pk_mov_b32 v[58:59], v[52:53], v[50:51] op_sel:[1,0]
	v_mov_b32_e32 v53, v51
	v_pk_mov_b32 v[50:51], v[48:49], v[46:47] op_sel:[1,0]
	v_mov_b32_e32 v49, v47
	s_cselect_b32 s0, s4, s14
	v_pk_fma_f32 v[46:47], v[28:29], v[28:29], v[54:55] op_sel_hi:[1,1,0]
	v_pk_fma_f32 v[54:55], v[30:31], v[30:31], v[56:57] op_sel_hi:[1,1,0]
	v_pk_add_f32 v[52:53], v[58:59], v[52:53]
	v_pk_add_f32 v[48:49], v[50:51], v[48:49]
	s_ashr_i32 s1, s0, 31
	v_mul_f32_e32 v46, v44, v44
	v_mul_f32_e32 v54, v45, v45
	v_pk_add_f32 v[44:45], v[52:53], v[52:53] op_sel_hi:[0,1]
	v_pk_add_f32 v[48:49], v[48:49], v[48:49] op_sel_hi:[0,1]
	s_lshl_b64 s[0:1], s[0:1], 12
	v_pk_add_f32 v[58:59], v[46:47], v[54:55]
	v_mul_f32_e32 v44, v42, v42
	v_mul_f32_e32 v48, v43, v43
	v_lshl_add_u64 v[54:55], v[32:33], 0, s[0:1]
	v_pk_add_f32 v[60:61], v[44:45], v[48:49]
	global_load_dwordx4 v[42:45], v[54:55], off
	global_load_dwordx4 v[46:49], v[54:55], off offset:1024
	global_load_dwordx4 v[50:53], v[54:55], off offset:2048
	s_nop 0
	global_load_dwordx4 v[54:57], v[54:55], off offset:3072
	v_pk_add_f32 v[58:59], v[58:59], v[60:61]
	s_mov_b32 s14, s4
	v_add_f32_e32 v58, v58, v59
	s_cmpk_gt_i32 s4, 0xfff
	s_nop 1
	v_add_f32_dpp v58, v58, v58 quad_perm:[1,0,3,2] row_mask:0xf bank_mask:0xf
	s_nop 1
	v_add_f32_dpp v58, v58, v58 quad_perm:[2,3,0,1] row_mask:0xf bank_mask:0xf
	s_nop 1
	v_add_f32_dpp v58, v58, v58 row_half_mirror row_mask:0xf bank_mask:0xf
	s_nop 1
	v_add_f32_dpp v58, v58, v58 row_mirror row_mask:0xf bank_mask:0xf
	v_mov_b32_e32 v59, v58
	s_nop 1
	v_permlane16_swap_b32_e32 v58, v59
	v_add_f32_e32 v58, v58, v59
	v_mov_b32_e32 v59, v58
	s_nop 1
	v_permlane32_swap_b32_e32 v58, v59
	v_add_f32_e32 v58, v58, v59
	v_fmamk_f32 v58, v58, 0x3a800000, v222
	v_mul_f32_e32 v59, 0x4f800000, v58
	v_cmp_gt_f32_e32 vcc, s78, v58
	s_nop 1
	v_cndmask_b32_e32 v58, v58, v59, vcc
	v_sqrt_f32_e32 v59, v58
	s_nop 0
	v_add_u32_e32 v60, -1, v59
	v_add_u32_e32 v61, 1, v59
	v_fma_f32 v62, -v60, v59, v58
	v_fma_f32 v63, -v61, v59, v58
	v_cmp_ge_f32_e64 s[0:1], 0, v62
	s_nop 1
	v_cndmask_b32_e64 v59, v59, v60, s[0:1]
	v_cmp_lt_f32_e64 s[0:1], 0, v63
	s_nop 1
	v_cndmask_b32_e64 v59, v59, v61, s[0:1]
	v_mul_f32_e32 v60, 0x37800000, v59
	v_cndmask_b32_e32 v59, v59, v60, vcc
	v_cmp_class_f32_e32 vcc, v58, v223
	s_nop 1
	v_cndmask_b32_e32 v58, v59, v58, vcc
	v_div_scale_f32 v59, s[0:1], v58, v58, 1.0
	v_rcp_f32_e32 v61, v59
	v_div_scale_f32 v60, vcc, 1.0, v58, 1.0
	v_fma_f32 v62, -v59, v61, 1.0
	v_fmac_f32_e32 v61, v62, v61
	v_mul_f32_e32 v62, v60, v61
	v_fma_f32 v63, -v59, v62, v60
	v_fmac_f32_e32 v62, v63, v61
	v_fma_f32 v59, -v59, v62, v60
	v_div_fmas_f32 v59, v59, v61, v62
	v_div_fixup_f32 v58, v59, v58, 1.0
	v_pk_mul_f32 v[16:17], v[16:17], v[58:59] op_sel_hi:[1,0]
	v_pk_mul_f32 v[18:19], v[18:19], v[58:59] op_sel_hi:[1,0]
	v_pk_mul_f32 v[20:21], v[20:21], v[58:59] op_sel_hi:[1,0]
	v_pk_mul_f32 v[22:23], v[22:23], v[58:59] op_sel_hi:[1,0]
	v_pk_mul_f32 v[28:29], v[28:29], v[58:59] op_sel_hi:[1,0]
	v_pk_mul_f32 v[30:31], v[30:31], v[58:59] op_sel_hi:[1,0]
	v_pk_mul_f32 v[24:25], v[24:25], v[58:59] op_sel_hi:[1,0]
	v_pk_mul_f32 v[26:27], v[26:27], v[58:59] op_sel_hi:[1,0]
	v_pk_mul_f32 v[18:19], v[2:3], v[18:19]
	v_pk_mul_f32 v[16:17], v[0:1], v[16:17]
	v_pk_mul_f32 v[22:23], v[6:7], v[22:23]
	v_pk_mul_f32 v[20:21], v[4:5], v[20:21]
	v_pk_mul_f32 v[30:31], v[10:11], v[30:31]
	v_pk_mul_f32 v[28:29], v[8:9], v[28:29]
	v_pk_mul_f32 v[26:27], v[14:15], v[26:27]
	v_pk_mul_f32 v[24:25], v[12:13], v[24:25]
	v_cvt_pk_bf16_f32 v16, v16, v17
	v_cvt_pk_bf16_f32 v17, v18, v19
	v_cvt_pk_bf16_f32 v18, v20, v21
	v_cvt_pk_bf16_f32 v19, v22, v23
	v_cvt_pk_bf16_f32 v20, v28, v29
	v_cvt_pk_bf16_f32 v21, v30, v31
	v_cvt_pk_bf16_f32 v22, v24, v25
	v_cvt_pk_bf16_f32 v23, v26, v27
	s_waitcnt vmcnt(0)
	v_mov_b64_e32 v[24:25], v[54:55]
	global_store_dwordx2 v[34:35], v[16:17], off
	global_store_dwordx2 v[34:35], v[18:19], off offset:512
	global_store_dwordx2 v[34:35], v[20:21], off offset:1024
	global_store_dwordx2 v[34:35], v[22:23], off offset:1536
	v_lshl_add_u64 v[34:35], v[34:35], 0, s[2:3]
	v_mov_b64_e32 v[26:27], v[56:57]
	v_mov_b32_e32 v16, v42
	v_mov_b32_e32 v17, v43
	v_mov_b32_e32 v18, v44
	v_mov_b32_e32 v19, v45
	v_mov_b32_e32 v20, v46
	v_mov_b32_e32 v21, v47
	v_mov_b32_e32 v22, v48
	v_mov_b32_e32 v23, v49
	v_mov_b32_e32 v28, v50
	v_mov_b32_e32 v29, v51
	v_mov_b32_e32 v30, v52
	v_mov_b32_e32 v31, v53
	v_mov_b32_e32 v44, v54
	v_mov_b32_e32 v45, v55
	v_mov_b32_e32 v42, v56
	v_mov_b32_e32 v43, v57
	s_cbranch_scc0 .LBB0_242
	s_load_dwordx8 s[36:43], s[92:93], 0x110

.LBB0_1710:
	s_add_i32 s0, s2, s5
	s_waitcnt vmcnt(3)
	v_lshlrev_b32_e32 v49, 16, v36
	s_waitcnt vmcnt(0)
	v_and_b32_e32 v51, 0xffff0000, v38
	v_and_b32_e32 v53, 0xffff0000, v39
	s_cmp_lt_i32 s0, 0x8000
	v_and_b32_e32 v29, 0xffff0000, v36
	v_lshlrev_b32_e32 v26, 16, v37
	v_and_b32_e32 v27, 0xffff0000, v37
	v_lshlrev_b32_e32 v50, 16, v38
	v_lshlrev_b32_e32 v52, 16, v39
	v_lshlrev_b32_e32 v55, 16, v35
	v_lshlrev_b32_e32 v54, 16, v34
	v_and_b32_e32 v57, 0xffff0000, v35
	v_and_b32_e32 v56, 0xffff0000, v34
	v_and_b32_e32 v61, 0xffff0000, v33
	v_mov_b64_e32 v[36:37], v[20:21]
	v_mov_b64_e32 v[34:35], v[24:25]
	v_mul_f32_e32 v20, v53, v53
	v_mul_f32_e32 v24, v51, v51
	v_mov_b32_e32 v21, v49
	s_cselect_b32 s8, s0, s2
	v_lshlrev_b32_e32 v58, 16, v32
	v_and_b32_e32 v59, 0xffff0000, v32
	v_lshlrev_b32_e32 v60, 16, v33
	v_mov_b64_e32 v[32:33], v[22:23]
	v_pk_mul_f32 v[22:23], v[56:57], v[56:57]
	v_mul_f32_e32 v48, v61, v61
	v_pk_fma_f32 v[64:65], v[52:53], v[52:53], v[20:21] op_sel_hi:[1,1,0]
	v_pk_fma_f32 v[24:25], v[50:51], v[50:51], v[24:25] op_sel_hi:[1,1,0]
	s_ashr_i32 s3, s2, 31
	s_ashr_i32 s9, s8, 31
	v_mov_b64_e32 v[38:39], v[30:31]
	v_mul_f32_e32 v30, v59, v59
	v_mov_b32_e32 v62, v54
	v_mov_b32_e32 v63, v56
	v_mov_b32_e32 v56, v55
	v_pk_fma_f32 v[22:23], v[54:55], v[54:55], v[22:23]
	v_pk_fma_f32 v[54:55], v[60:61], v[60:61], v[48:49] op_sel_hi:[1,1,0]
	v_mov_b32_e32 v48, v24
	v_mov_b32_e32 v20, v64
	s_lshl_b64 s[10:11], s[2:3], 12
	s_sub_i32 s2, s0, s4
	s_lshl_b64 s[0:1], s[8:9], 11
	v_mul_f32_e32 v66, v29, v29
	v_mul_f32_e32 v67, v26, v26
	v_mul_f32_e32 v68, v27, v27
	v_mov_b32_e32 v28, v49
	v_pk_fma_f32 v[30:31], v[58:59], v[58:59], v[30:31] op_sel_hi:[1,1,0]
	v_pk_add_f32 v[22:23], v[22:23], v[22:23] op_sel:[0,1] op_sel_hi:[1,0]
	v_pk_mul_f32 v[20:21], v[48:49], v[20:21]
	v_lshl_add_u64 v[48:49], v[16:17], 0, s[0:1]
	v_pk_add_f32 v[24:25], v[24:25], v[64:65]
	v_mov_b32_e32 v31, v67
	v_mov_b32_e32 v55, v68
	v_mov_b32_e32 v23, v66
	global_load_dwordx2 v[64:65], v[48:49], off
	global_load_dwordx2 v[66:67], v[48:49], off offset:512
	global_load_dwordx2 v[68:69], v[48:49], off offset:1024
	global_load_dwordx2 v[70:71], v[48:49], off offset:1536
	v_mov_b32_e32 v25, v21
	v_pk_add_f32 v[30:31], v[30:31], v[54:55]
	v_pk_add_f32 v[20:21], v[24:25], v[22:23]
	v_lshl_add_u64 v[54:55], v[18:19], 0, s[10:11]
	v_pk_add_f32 v[20:21], v[20:21], v[30:31]
	s_cmp_lt_i32 s2, 0x8000
	v_add_f32_e32 v20, v20, v21
	s_nop 1
	v_add_f32_dpp v20, v20, v20 quad_perm:[1,0,3,2] row_mask:0xf bank_mask:0xf
	s_nop 1
	v_add_f32_dpp v20, v20, v20 quad_perm:[2,3,0,1] row_mask:0xf bank_mask:0xf
	s_nop 1
	v_add_f32_dpp v20, v20, v20 row_half_mirror row_mask:0xf bank_mask:0xf
	s_nop 1
	v_add_f32_dpp v20, v20, v20 row_mirror row_mask:0xf bank_mask:0xf
	v_mov_b32_e32 v21, v20
	s_nop 1
	v_permlane16_swap_b32_e32 v20, v21
	v_add_f32_e32 v20, v20, v21
	v_mov_b32_e32 v21, v20
	s_nop 1
	v_permlane32_swap_b32_e32 v20, v21
	v_add_f32_e32 v20, v20, v21
	v_fmamk_f32 v20, v20, 0x3a800000, v46
	v_mul_f32_e32 v21, 0x4f800000, v20
	v_cmp_gt_f32_e32 vcc, s6, v20
	s_nop 1
	v_cndmask_b32_e32 v20, v20, v21, vcc
	v_sqrt_f32_e32 v21, v20
	s_nop 0
	v_add_u32_e32 v22, -1, v21
	v_add_u32_e32 v23, 1, v21
	v_fma_f32 v24, -v22, v21, v20
	v_fma_f32 v25, -v23, v21, v20
	v_cmp_ge_f32_e64 s[0:1], 0, v24
	s_nop 1
	v_cndmask_b32_e64 v21, v21, v22, s[0:1]
	v_cmp_lt_f32_e64 s[0:1], 0, v25
	s_nop 1
	v_cndmask_b32_e64 v21, v21, v23, s[0:1]
	v_mul_f32_e32 v22, 0x37800000, v21
	v_cndmask_b32_e32 v21, v21, v22, vcc
	v_cmp_class_f32_e32 vcc, v20, v47
	s_nop 1
	v_cndmask_b32_e32 v20, v21, v20, vcc
	v_div_scale_f32 v21, s[0:1], v20, v20, 1.0
	v_rcp_f32_e32 v23, v21
	v_div_scale_f32 v22, vcc, 1.0, v20, 1.0
	v_fma_f32 v24, -v21, v23, 1.0
	v_fmac_f32_e32 v23, v24, v23
	v_mul_f32_e32 v24, v22, v23
	v_fma_f32 v25, -v21, v24, v22
	v_fmac_f32_e32 v24, v25, v23
	v_fma_f32 v21, -v21, v24, v22
	v_div_fmas_f32 v21, v21, v23, v24
	v_div_fixup_f32 v20, v21, v20, 1.0
	v_pk_mul_f32 v[24:25], v[20:21], v[50:51] op_sel_hi:[0,1]
	v_pk_mul_f32 v[22:23], v[20:21], v[52:53] op_sel_hi:[0,1]
	v_pk_mul_f32 v[30:31], v[20:21], v[62:63] op_sel_hi:[0,1]
	v_pk_mul_f32 v[52:53], v[20:21], v[60:61] op_sel_hi:[0,1]
	v_pk_mul_f32 v[48:49], v[20:21], v[56:57] op_sel_hi:[0,1]
	v_pk_mul_f32 v[50:51], v[20:21], v[58:59] op_sel_hi:[0,1]
	v_pk_mul_f32 v[56:57], v[20:21], v[28:29] op_sel_hi:[0,1]
	v_pk_mul_f32 v[58:59], v[20:21], v[26:27] op_sel_hi:[0,1]
	v_pk_mul_f32 v[22:23], v[22:23], v[2:3]
	v_pk_mul_f32 v[20:21], v[24:25], v[0:1]
	v_pk_mul_f32 v[24:25], v[30:31], v[4:5]
	v_pk_mul_f32 v[30:31], v[52:53], v[10:11]
	v_pk_mul_f32 v[26:27], v[48:49], v[6:7]
	v_pk_mul_f32 v[28:29], v[50:51], v[8:9]
	v_pk_mul_f32 v[50:51], v[58:59], v[14:15]
	v_pk_mul_f32 v[48:49], v[56:57], v[12:13]
	global_store_dwordx4 v[54:55], v[20:23], off
	global_store_dwordx4 v[54:55], v[24:27], off offset:1024
	global_store_dwordx4 v[54:55], v[28:31], off offset:2048
	global_store_dwordx4 v[54:55], v[48:51], off offset:3072
	s_waitcnt vmcnt(4)
	v_mov_b64_e32 v[20:21], v[70:71]
	v_mov_b64_e32 v[22:23], v[68:69]
	v_mov_b64_e32 v[24:25], v[66:67]
	v_mov_b64_e32 v[30:31], v[64:65]
	s_cbranch_scc1 .LBB0_1710
